# MLA steady loops: K-piece count resolved per wave group, DMA LDS targets (m0) prepared in the QK section's MFMA gaps of the previous iteration
# speedup vs baseline: 1.0094x; 1.0094x over previous
; #define ISSUE_K(t, sl) do { glds16(Kg + (long)(t) * (KSLOT / 2), (unsigned)__builtin_amdgcn_readfirstlane(kdst + (sl) * KSLOT)); \
;         if (k2) glds16(Kg + (long)(t) * (KSLOT / 2) + 4096, (unsigned)__builtin_amdgcn_readfirstlane(kdst + (sl) * KSLOT + 8192)); } while (0)
; #define ISSUE_V(t, sl) glds16(Vg + (long)(t) * 4096, (unsigned)__builtin_amdgcn_readfirstlane(vdst + (sl) * VSLOT))
; #define SFENCE() __builtin_amdgcn_sched_barrier(0)
; template <bool FOX>
; __device__ __forceinline__ void attn_unit(const Args& A, int b, int h, int qb, LAS char* shm, LAS float* dg) {
;     ...
;     const int t_end = (tw_last - t0 + 2 < nti) ? tw_last - t0 + 2 : nti;
; #pragma unroll 1
;     for (int t = 1; t < t_end; ++t) {
;         if (t == 1 && 4 < nti) ISSUE_K(t0 + 4, 0);
;         if (t + 4 < nti) ISSUE_K(t0 + t + 4, t % NS);
;         if (t + 2 < nti) ISSUE_V(t0 + t + 2, (t + 2) % NS);
;         SFENCE();
.LBB0_825:
	s_add_i32 s27, s26, 3
	s_cmp_lt_u32 s27, s94
	s_cbranch_scc0 .LBB0_828
	s_cmp_lg_u32 s98, 0
	s_cbranch_scc0 .Lmla_ss_no
	s_cmp_lg_u32 s26, s59
	s_cbranch_scc0 .Lmla_ss_no
	s_and_b32 s52, s27, 3
	s_mulk_i32 s52, 0x3000
	s_add_i32 s52, s52, s91
	s_add_i32 s53, s42, 0x6000
	s_and_b32 s53, s53, 0x6000
	s_add_i32 s53, s53, s93
	s_cmp_lt_i32 s89, 4
	s_cbranch_scc1 .Lmla_ss1_top
	s_branch .Lmla_ss2_top

; template <bool FOX>
; __device__ __forceinline__ void attn_unit(const Args& A, int b, int h, int qb, LAS char* shm, LAS float* dg) {
;     ...
;     for (int t = 1; t < t_end; ++t) {
;         if (t == 1 && 4 < nti) ISSUE_K(t0 + 4, 0);
;         if (t + 4 < nti) ISSUE_K(t0 + t + 4, t % NS);
;         if (t + 2 < nti) ISSUE_V(t0 + t + 2, (t + 2) % NS);
;         SFENCE();
;         { if constexpr (!FOX) { if (t0 + t == tw_last + 1) {
; #pragma unroll
;                   for (int r = 0; r < 16; ++r) negm[r] = -INFINITY;
;                   asm volatile("" : "+v"(negm)); } }
;           const lds_cptr vp = vp0 + ((t - 1) % NS) * VSLOT; float sa = 0.f, sb = 0.f;
; #pragma unroll
;           for (int g = 0; g < 2 * NQ; ++g) {
;               if (!FOX && g == 0) c0 = __builtin_amdgcn_mfma_f32_32x32x16_bf16(kf[0], qr[0], negm, 0, 0, 0);
;               else if (!FOX && g == 1) c1 = __builtin_amdgcn_mfma_f32_32x32x16_bf16(kf[1], qr[0], negm, 0, 0, 0);
;               else if (g & 1) c1 = __builtin_amdgcn_mfma_f32_32x32x16_bf16(kf[g], qr[g >> 1], c1, 0, 0, 0); else c0 = __builtin_amdgcn_mfma_f32_32x32x16_bf16(kf[g], qr[g >> 1], c0, 0, 0, 0);
;               if (g < 8) { const int i = (g >> 1) + 4 * (g & 1); vlo[i] = vtr(vp + (i >> 2) * 4096 + (i & 3) * 1024); vhi[i] = vtr(vp + (i >> 2) * 4096 + (i & 3) * 1024 + 512);
;                   if (g < 4) { sa += pp0[4 * g]; sb += pp0[4 * g + 1]; sa += pp0[4 * g + 2]; sb += pp0[4 * g + 3]; } else { sa += pp1[4 * g - 16]; sb += pp1[4 * g - 15]; sa += pp1[4 * g - 14]; sb += pp1[4 * g - 13]; }
;                   asm volatile("" : "+v"(sa), "+v"(sb)); }
;               { constexpr int G0 = FOX ? 0 : 4; if (g >= G0) { const int q = 2 * (g - G0);
; #pragma unroll
;                   for (int k = 0; k < 2; ++k) { const int w = q + k; const unsigned pkd = w < 8 ? cvt_pk_bf16(pp0[2 * w], pp0[2 * w + 1]) : cvt_pk_bf16(pp1[2 * w - 16], pp1[2 * w - 15]); pw[w >> 2][w & 3] = pkd; } } }
;               SFENCE();
;           }
;           lrun += sa + sb; }
;         MASKONLY(t);
;         float rm; ROWMAX(rm);
;         bool resc = false;
;         if (__any(rm > THR)) { const float dl = fmaxf(rm, 0.f); mhat += dl;
; #pragma unroll
;             for (int r = 0; r < 16; ++r) { c0[r] -= dl; c1[r] -= dl; }
;             if constexpr (!FOX) {
; #pragma unroll
;                 for (int r = 0; r < 16; ++r) negm[r] = -mhat;
.Lmla_ss1_top:
	s_mov_b32 m0, s52
	v_lshl_add_u64 v[4:5], v[234:235], 0, s[56:57]
	global_load_lds_dwordx4 v[234:235], off
	s_add_i32 m0, s52, 0x2000
	s_nop 0
	global_load_lds_dwordx4 v[4:5], off
	s_mov_b32 m0, s53
	v_lshl_add_u64 v[4:5], v[232:233], 0, s[42:43]
	global_load_lds_dwordx4 v[4:5], off
	s_waitcnt lgkmcnt(0)
	s_add_i32 s27, s42, 0x8000
	v_mfma_f32_32x32x16_bf16 v[114:129], v[206:209], v[138:141], v[82:97]
	s_and_b32 s27, s27, 0x6000
	v_add_u32_e32 v3, s27, v247
	ds_read_b64_tr_b16 v[206:207], v3 offset:49152
	ds_read_b64_tr_b16 v[208:209], v3 offset:49664
	v_add_f32_e32 v4, 0, v67
	v_add_f32_e32 v5, 0, v66
	v_add_f32_e32 v4, v69, v4
	v_add_f32_e32 v5, v68, v5
	v_mfma_f32_32x32x16_bf16 v[98:113], v[194:197], v[138:141], v[82:97]
	ds_read_b64_tr_b16 v[194:195], v3 offset:53248
	ds_read_b64_tr_b16 v[196:197], v3 offset:53760
	v_add_f32_e32 v4, v71, v4
	v_add_f32_e32 v5, v70, v5
	v_add_f32_e32 v4, v73, v4
	v_add_f32_e32 v5, v72, v5
	v_mfma_f32_32x32x16_bf16 v[114:129], v[202:205], v[142:145], v[114:129]
	ds_read_b64_tr_b16 v[202:203], v3 offset:50176
	ds_read_b64_tr_b16 v[204:205], v3 offset:50688
	v_add_f32_e32 v4, v75, v4
	v_add_f32_e32 v5, v74, v5
	v_add_f32_e32 v4, v77, v4
	v_add_f32_e32 v5, v76, v5
	v_mfma_f32_32x32x16_bf16 v[98:113], v[186:189], v[142:145], v[98:113]
	ds_read_b64_tr_b16 v[214:215], v3 offset:54272
	ds_read_b64_tr_b16 v[216:217], v3 offset:54784
	v_add_f32_e32 v4, v79, v4
	v_add_f32_e32 v5, v78, v5
	v_add_f32_e32 v4, v81, v4
	v_add_f32_e32 v5, v80, v5
	v_mfma_f32_32x32x16_bf16 v[114:129], v[198:201], v[146:149], v[114:129]
	ds_read_b64_tr_b16 v[210:211], v3 offset:51200
	ds_read_b64_tr_b16 v[212:213], v3 offset:51712
	v_add_f32_e32 v4, v51, v4
	v_add_f32_e32 v5, v50, v5
	v_add_f32_e32 v4, v53, v4
	v_add_f32_e32 v5, v52, v5
	v_mfma_f32_32x32x16_bf16 v[98:113], v[182:185], v[146:149], v[98:113]
	ds_read_b64_tr_b16 v[12:13], v3 offset:55296
	ds_read_b64_tr_b16 v[14:15], v3 offset:55808
	v_add_f32_e32 v4, v55, v4
	v_add_f32_e32 v5, v54, v5
	v_add_f32_e32 v4, v57, v4
	v_add_f32_e32 v5, v56, v5
	v_mfma_f32_32x32x16_bf16 v[114:129], v[190:193], v[150:153], v[114:129]
	ds_read_b64_tr_b16 v[8:9], v3 offset:52224
	ds_read_b64_tr_b16 v[10:11], v3 offset:52736
	v_add_f32_e32 v4, v59, v4
	v_add_f32_e32 v16, v61, v4
	v_add_f32_e32 v4, v58, v5
	v_add_f32_e32 v17, v60, v4
	v_mfma_f32_32x32x16_bf16 v[98:113], v[170:173], v[150:153], v[98:113]
	s_and_b32 s64, s26, 3
	ds_read_b64_tr_b16 v[4:5], v3 offset:56320
	ds_read_b64_tr_b16 v[6:7], v3 offset:56832
	v_add_f32_e32 v3, v63, v16
	v_add_f32_e32 v16, v62, v17
	v_add_f32_e32 v3, v65, v3
	v_add_f32_e32 v16, v64, v16
	v_mfma_f32_32x32x16_bf16 v[114:129], v[178:181], v[154:157], v[114:129]
	s_mulk_i32 s64, 0x3000
	v_cvt_pk_bf16_f32 v178, v50, v51
	v_cvt_pk_bf16_f32 v179, v52, v53
	v_cvt_pk_bf16_f32 v186, v66, v67
	v_cvt_pk_bf16_f32 v187, v68, v69
	v_mfma_f32_32x32x16_bf16 v[98:113], v[166:169], v[154:157], v[98:113]
	s_add_i32 s52, s64, s91
	s_and_b32 s64, s42, 0x6000
	v_cvt_pk_bf16_f32 v180, v54, v55
	v_cvt_pk_bf16_f32 v181, v56, v57
	v_cvt_pk_bf16_f32 v188, v70, v71
	v_cvt_pk_bf16_f32 v189, v72, v73
	v_mfma_f32_32x32x16_bf16 v[114:129], v[174:177], v[158:161], v[114:129]
	s_add_i32 s53, s64, s93
	v_cvt_pk_bf16_f32 v218, v58, v59
	v_cvt_pk_bf16_f32 v219, v60, v61
	v_cvt_pk_bf16_f32 v182, v74, v75
	v_cvt_pk_bf16_f32 v183, v76, v77
	v_mfma_f32_32x32x16_bf16 v[98:113], v[162:165], v[158:161], v[98:113]
	v_cvt_pk_bf16_f32 v220, v62, v63
	v_cvt_pk_bf16_f32 v221, v64, v65
	v_cvt_pk_bf16_f32 v184, v78, v79
	v_cvt_pk_bf16_f32 v185, v80, v81
	v_add_f32_e32 v3, v3, v16
	v_add_f32_e32 v246, v246, v3
	s_nop 3
	s_waitcnt lgkmcnt(0)
	v_mfma_f32_32x32x16_bf16 v[18:33], v[186:189], v[206:209], v[18:33]
	s_add_i32 s27, s26, 1
	s_and_b32 s64, s27, 3
	s_mulk_i32 s64, 0x3000
	v_exp_f32_e32 v66, v114
	v_exp_f32_e32 v67, v115
	v_exp_f32_e32 v68, v116
	v_exp_f32_e32 v69, v117
	v_add_u32_e32 v3, s64, v248
	v_mfma_f32_32x32x16_bf16 v[34:49], v[186:189], v[194:197], v[34:49]
	v_exp_f32_e32 v70, v118
	v_exp_f32_e32 v71, v119
	v_exp_f32_e32 v72, v120
	v_exp_f32_e32 v73, v121
	ds_read_b128 v[206:209], v3
	ds_read_b128 v[194:197], v3 offset:512
	v_mfma_f32_32x32x16_bf16 v[18:33], v[182:185], v[202:205], v[18:33]
	v_exp_f32_e32 v74, v122
	v_exp_f32_e32 v75, v123
	v_exp_f32_e32 v76, v124
	v_exp_f32_e32 v77, v125
	ds_read_b128 v[202:205], v3 offset:2048
	ds_read_b128 v[186:189], v3 offset:2560
	v_mfma_f32_32x32x16_bf16 v[34:49], v[182:185], v[214:217], v[34:49]
	v_exp_f32_e32 v78, v126
	v_exp_f32_e32 v79, v127
	v_exp_f32_e32 v80, v128
	v_exp_f32_e32 v81, v129
	ds_read_b128 v[198:201], v3 offset:4096
	ds_read_b128 v[182:185], v3 offset:4608
	v_mfma_f32_32x32x16_bf16 v[18:33], v[178:181], v[210:213], v[18:33]
	v_exp_f32_e32 v50, v98
	v_exp_f32_e32 v51, v99
	v_exp_f32_e32 v52, v100
	v_exp_f32_e32 v53, v101
	ds_read_b128 v[190:193], v3 offset:6144
	ds_read_b128 v[170:173], v3 offset:6656
	v_mfma_f32_32x32x16_bf16 v[34:49], v[178:181], v[12:15], v[34:49]
	v_exp_f32_e32 v54, v102
	v_exp_f32_e32 v55, v103
	v_exp_f32_e32 v56, v104
	v_exp_f32_e32 v57, v105
	ds_read_b128 v[178:181], v3 offset:8192
	ds_read_b128 v[166:169], v3 offset:8704
	v_mfma_f32_32x32x16_bf16 v[18:33], v[218:221], v[8:11], v[18:33]
	v_exp_f32_e32 v58, v106
	v_exp_f32_e32 v59, v107
	v_exp_f32_e32 v60, v108
	v_exp_f32_e32 v61, v109
	ds_read_b128 v[174:177], v3 offset:10240
	ds_read_b128 v[162:165], v3 offset:10752
	v_mfma_f32_32x32x16_bf16 v[34:49], v[218:221], v[4:7], v[34:49]
	v_exp_f32_e32 v62, v110
	v_exp_f32_e32 v63, v111
	v_exp_f32_e32 v64, v112
	v_exp_f32_e32 v65, v113
	s_waitcnt vmcnt(4)
	s_barrier
	s_add_u32 s42, s42, 0x2000
	s_addc_u32 s43, s43, 0
	v_lshl_add_u64 v[234:235], v[234:235], 0, s[62:63]
	s_cmp_eq_u32 s27, s96
	s_cbranch_scc1 .Lmla_ss_done
	s_mov_b32 s26, s27
	s_add_i32 s64, s26, 3
	s_cmp_lt_u32 s64, s94
	s_cbranch_scc1 .Lmla_ss1_top
	s_branch .Lmla_ss_back
; template <bool FOX>
; __device__ __forceinline__ void attn_unit(const Args& A, int b, int h, int qb, LAS char* shm, LAS float* dg) {
;     ...
;     for (int t = 1; t < t_end; ++t) {
;         if (t == 1 && 4 < nti) ISSUE_K(t0 + 4, 0);
;         if (t + 4 < nti) ISSUE_K(t0 + t + 4, t % NS);
;         if (t + 2 < nti) ISSUE_V(t0 + t + 2, (t + 2) % NS);
;         SFENCE();
;         { if constexpr (!FOX) { if (t0 + t == tw_last + 1) {
; #pragma unroll
;                   for (int r = 0; r < 16; ++r) negm[r] = -INFINITY;
;                   asm volatile("" : "+v"(negm)); } }
;           const lds_cptr vp = vp0 + ((t - 1) % NS) * VSLOT; float sa = 0.f, sb = 0.f;
; #pragma unroll
;           for (int g = 0; g < 2 * NQ; ++g) {
;               if (!FOX && g == 0) c0 = __builtin_amdgcn_mfma_f32_32x32x16_bf16(kf[0], qr[0], negm, 0, 0, 0);
;               else if (!FOX && g == 1) c1 = __builtin_amdgcn_mfma_f32_32x32x16_bf16(kf[1], qr[0], negm, 0, 0, 0);
;               else if (g & 1) c1 = __builtin_amdgcn_mfma_f32_32x32x16_bf16(kf[g], qr[g >> 1], c1, 0, 0, 0); else c0 = __builtin_amdgcn_mfma_f32_32x32x16_bf16(kf[g], qr[g >> 1], c0, 0, 0, 0);
;               if (g < 8) { const int i = (g >> 1) + 4 * (g & 1); vlo[i] = vtr(vp + (i >> 2) * 4096 + (i & 3) * 1024); vhi[i] = vtr(vp + (i >> 2) * 4096 + (i & 3) * 1024 + 512);
;                   if (g < 4) { sa += pp0[4 * g]; sb += pp0[4 * g + 1]; sa += pp0[4 * g + 2]; sb += pp0[4 * g + 3]; } else { sa += pp1[4 * g - 16]; sb += pp1[4 * g - 15]; sa += pp1[4 * g - 14]; sb += pp1[4 * g - 13]; }
;                   asm volatile("" : "+v"(sa), "+v"(sb)); }
;               { constexpr int G0 = FOX ? 0 : 4; if (g >= G0) { const int q = 2 * (g - G0);
; #pragma unroll
;                   for (int k = 0; k < 2; ++k) { const int w = q + k; const unsigned pkd = w < 8 ? cvt_pk_bf16(pp0[2 * w], pp0[2 * w + 1]) : cvt_pk_bf16(pp1[2 * w - 16], pp1[2 * w - 15]); pw[w >> 2][w & 3] = pkd; } } }
;               SFENCE();
;           }
;           lrun += sa + sb; }
;         MASKONLY(t);
;         float rm; ROWMAX(rm);
;         bool resc = false;
;         if (__any(rm > THR)) { const float dl = fmaxf(rm, 0.f); mhat += dl;
; #pragma unroll
;             for (int r = 0; r < 16; ++r) { c0[r] -= dl; c1[r] -= dl; }
;             if constexpr (!FOX) {
; #pragma unroll
;                 for (int r = 0; r < 16; ++r) negm[r] = -mhat;
.Lmla_ss2_top:
	s_mov_b32 m0, s52
	s_nop 0
	global_load_lds_dwordx4 v[234:235], off
	s_mov_b32 m0, s53
	v_lshl_add_u64 v[4:5], v[232:233], 0, s[42:43]
	global_load_lds_dwordx4 v[4:5], off
	s_waitcnt lgkmcnt(0)
	s_add_i32 s27, s42, 0x8000
	v_mfma_f32_32x32x16_bf16 v[114:129], v[206:209], v[138:141], v[82:97]
	s_and_b32 s27, s27, 0x6000
	v_add_u32_e32 v3, s27, v247
	ds_read_b64_tr_b16 v[206:207], v3 offset:49152
	ds_read_b64_tr_b16 v[208:209], v3 offset:49664
	v_add_f32_e32 v4, 0, v67
	v_add_f32_e32 v5, 0, v66
	v_add_f32_e32 v4, v69, v4
	v_add_f32_e32 v5, v68, v5
	v_mfma_f32_32x32x16_bf16 v[98:113], v[194:197], v[138:141], v[82:97]
	ds_read_b64_tr_b16 v[194:195], v3 offset:53248
	ds_read_b64_tr_b16 v[196:197], v3 offset:53760
	v_add_f32_e32 v4, v71, v4
	v_add_f32_e32 v5, v70, v5
	v_add_f32_e32 v4, v73, v4
	v_add_f32_e32 v5, v72, v5
	v_mfma_f32_32x32x16_bf16 v[114:129], v[202:205], v[142:145], v[114:129]
	ds_read_b64_tr_b16 v[202:203], v3 offset:50176
	ds_read_b64_tr_b16 v[204:205], v3 offset:50688
	v_add_f32_e32 v4, v75, v4
	v_add_f32_e32 v5, v74, v5
	v_add_f32_e32 v4, v77, v4
	v_add_f32_e32 v5, v76, v5
	v_mfma_f32_32x32x16_bf16 v[98:113], v[186:189], v[142:145], v[98:113]
	ds_read_b64_tr_b16 v[214:215], v3 offset:54272
	ds_read_b64_tr_b16 v[216:217], v3 offset:54784
	v_add_f32_e32 v4, v79, v4
	v_add_f32_e32 v5, v78, v5
	v_add_f32_e32 v4, v81, v4
	v_add_f32_e32 v5, v80, v5
	v_mfma_f32_32x32x16_bf16 v[114:129], v[198:201], v[146:149], v[114:129]
	ds_read_b64_tr_b16 v[210:211], v3 offset:51200
	ds_read_b64_tr_b16 v[212:213], v3 offset:51712
	v_add_f32_e32 v4, v51, v4
	v_add_f32_e32 v5, v50, v5
	v_add_f32_e32 v4, v53, v4
	v_add_f32_e32 v5, v52, v5
	v_mfma_f32_32x32x16_bf16 v[98:113], v[182:185], v[146:149], v[98:113]
	ds_read_b64_tr_b16 v[12:13], v3 offset:55296
	ds_read_b64_tr_b16 v[14:15], v3 offset:55808
	v_add_f32_e32 v4, v55, v4
	v_add_f32_e32 v5, v54, v5
	v_add_f32_e32 v4, v57, v4
	v_add_f32_e32 v5, v56, v5
	v_mfma_f32_32x32x16_bf16 v[114:129], v[190:193], v[150:153], v[114:129]
	ds_read_b64_tr_b16 v[8:9], v3 offset:52224
	ds_read_b64_tr_b16 v[10:11], v3 offset:52736
	v_add_f32_e32 v4, v59, v4
	v_add_f32_e32 v16, v61, v4
	v_add_f32_e32 v4, v58, v5
	v_add_f32_e32 v17, v60, v4
	v_mfma_f32_32x32x16_bf16 v[98:113], v[170:173], v[150:153], v[98:113]
	s_and_b32 s64, s26, 3
	ds_read_b64_tr_b16 v[4:5], v3 offset:56320
	ds_read_b64_tr_b16 v[6:7], v3 offset:56832
	v_add_f32_e32 v3, v63, v16
	v_add_f32_e32 v16, v62, v17
	v_add_f32_e32 v3, v65, v3
	v_add_f32_e32 v16, v64, v16
	v_mfma_f32_32x32x16_bf16 v[114:129], v[178:181], v[154:157], v[114:129]
	s_mulk_i32 s64, 0x3000
	v_cvt_pk_bf16_f32 v178, v50, v51
	v_cvt_pk_bf16_f32 v179, v52, v53
	v_cvt_pk_bf16_f32 v186, v66, v67
	v_cvt_pk_bf16_f32 v187, v68, v69
	v_mfma_f32_32x32x16_bf16 v[98:113], v[166:169], v[154:157], v[98:113]
	s_add_i32 s52, s64, s91
	s_and_b32 s64, s42, 0x6000
	v_cvt_pk_bf16_f32 v180, v54, v55
	v_cvt_pk_bf16_f32 v181, v56, v57
	v_cvt_pk_bf16_f32 v188, v70, v71
	v_cvt_pk_bf16_f32 v189, v72, v73
	v_mfma_f32_32x32x16_bf16 v[114:129], v[174:177], v[158:161], v[114:129]
	s_add_i32 s53, s64, s93
	v_cvt_pk_bf16_f32 v218, v58, v59
	v_cvt_pk_bf16_f32 v219, v60, v61
	v_cvt_pk_bf16_f32 v182, v74, v75
	v_cvt_pk_bf16_f32 v183, v76, v77
	v_mfma_f32_32x32x16_bf16 v[98:113], v[162:165], v[158:161], v[98:113]
	v_cvt_pk_bf16_f32 v220, v62, v63
	v_cvt_pk_bf16_f32 v221, v64, v65
	v_cvt_pk_bf16_f32 v184, v78, v79
	v_cvt_pk_bf16_f32 v185, v80, v81
	v_add_f32_e32 v3, v3, v16
	v_add_f32_e32 v246, v246, v3
	s_waitcnt vmcnt(3)
	s_waitcnt lgkmcnt(0)
	s_barrier
	v_mfma_f32_32x32x16_bf16 v[18:33], v[186:189], v[206:209], v[18:33]
	s_add_i32 s27, s26, 1
	s_and_b32 s64, s27, 3
	s_mulk_i32 s64, 0x3000
	v_exp_f32_e32 v66, v114
	v_exp_f32_e32 v67, v115
	v_exp_f32_e32 v68, v116
	v_exp_f32_e32 v69, v117
	v_add_u32_e32 v3, s64, v248
	v_mfma_f32_32x32x16_bf16 v[34:49], v[186:189], v[194:197], v[34:49]
	v_exp_f32_e32 v70, v118
	v_exp_f32_e32 v71, v119
	v_exp_f32_e32 v72, v120
	v_exp_f32_e32 v73, v121
	ds_read_b128 v[206:209], v3
	ds_read_b128 v[194:197], v3 offset:512
	v_mfma_f32_32x32x16_bf16 v[18:33], v[182:185], v[202:205], v[18:33]
	v_exp_f32_e32 v74, v122
	v_exp_f32_e32 v75, v123
	v_exp_f32_e32 v76, v124
	v_exp_f32_e32 v77, v125
	ds_read_b128 v[202:205], v3 offset:2048
	ds_read_b128 v[186:189], v3 offset:2560
	v_mfma_f32_32x32x16_bf16 v[34:49], v[182:185], v[214:217], v[34:49]
	v_exp_f32_e32 v78, v126
	v_exp_f32_e32 v79, v127
	v_exp_f32_e32 v80, v128
	v_exp_f32_e32 v81, v129
	ds_read_b128 v[198:201], v3 offset:4096
	ds_read_b128 v[182:185], v3 offset:4608
	v_mfma_f32_32x32x16_bf16 v[18:33], v[178:181], v[210:213], v[18:33]
	v_exp_f32_e32 v50, v98
	v_exp_f32_e32 v51, v99
	v_exp_f32_e32 v52, v100
	v_exp_f32_e32 v53, v101
	ds_read_b128 v[190:193], v3 offset:6144
	ds_read_b128 v[170:173], v3 offset:6656
	v_mfma_f32_32x32x16_bf16 v[34:49], v[178:181], v[12:15], v[34:49]
	v_exp_f32_e32 v54, v102
	v_exp_f32_e32 v55, v103
	v_exp_f32_e32 v56, v104
	v_exp_f32_e32 v57, v105
	ds_read_b128 v[178:181], v3 offset:8192
	ds_read_b128 v[166:169], v3 offset:8704
	v_mfma_f32_32x32x16_bf16 v[18:33], v[218:221], v[8:11], v[18:33]
	v_exp_f32_e32 v58, v106
	v_exp_f32_e32 v59, v107
	v_exp_f32_e32 v60, v108
	v_exp_f32_e32 v61, v109
	ds_read_b128 v[174:177], v3 offset:10240
	ds_read_b128 v[162:165], v3 offset:10752
	v_mfma_f32_32x32x16_bf16 v[34:49], v[218:221], v[4:7], v[34:49]
	v_exp_f32_e32 v62, v110
	v_exp_f32_e32 v63, v111
	v_exp_f32_e32 v64, v112
	v_exp_f32_e32 v65, v113
	s_add_u32 s42, s42, 0x2000
	s_addc_u32 s43, s43, 0
	v_lshl_add_u64 v[234:235], v[234:235], 0, s[62:63]
	s_cmp_eq_u32 s27, s96
	s_cbranch_scc1 .Lmla_ss_done
	s_mov_b32 s26, s27
	s_add_i32 s64, s26, 3
	s_cmp_lt_u32 s64, s94
	s_cbranch_scc1 .Lmla_ss2_top
	s_branch .Lmla_ss_back
